# k_fine run staging via LDS-DMA (global_load_lds_dword with M0 = run offset; VGPR staging + 16 ds_write blocks removed)
# baseline (speedup 1.0000x reference)
.LBB0_36:
	s_and_b64 vcc, exec, s[0:1]
	s_cbranch_vccz .LBB0_175
	v_lshrrev_b32_e32 v8, 2, v0
	v_and_b32_e32 v38, 0xf0, v8
	v_and_or_b32 v2, v0, 15, v38
	v_lshlrev_b32_e32 v4, 2, v2
	ds_read2st64_b32 v[2:3], v4 offset0:112 offset1:116
	ds_read_b32 v39, v4 offset:30720
	v_mov_b32_e32 v6, 0
	v_mov_b32_e32 v7, 0
	v_lshlrev_b32_e32 v4, 2, v1
	s_waitcnt lgkmcnt(0)
	v_mul_u32_u24_e32 v5, 0x186c, v38
	v_lshl_add_u32 v50, v5, 2, v4
	v_readlane_b32 s22, v2, 0
	v_readlane_b32 s0, v3, 0
	v_readlane_b32 s3, v39, 0
	s_lshl_b32 s22, s22, 2
	s_nop 0
	s_lshl_b32 m0, s3, 2
	v_cmp_gt_i32_e32 vcc, s0, v1
	v_add_u32_e32 v51, s22, v50
	s_and_saveexec_b64 s[0:1], vcc
	global_load_lds_dword v51, s[20:21]
	s_mov_b64 exec, s[0:1]
	v_readlane_b32 s22, v2, 1
	v_readlane_b32 s0, v3, 1
	v_readlane_b32 s3, v39, 1
	s_lshl_b32 s22, s22, 2
	s_add_u32 s22, s22, 0x61b0
	s_lshl_b32 m0, s3, 2
	v_cmp_gt_i32_e32 vcc, s0, v1
	v_add_u32_e32 v51, s22, v50
	s_and_saveexec_b64 s[0:1], vcc
	global_load_lds_dword v51, s[20:21]
	s_mov_b64 exec, s[0:1]
	v_readlane_b32 s22, v2, 2
	v_readlane_b32 s0, v3, 2
	v_readlane_b32 s3, v39, 2
	s_lshl_b32 s22, s22, 2
	s_add_u32 s22, s22, 0xc360
	s_lshl_b32 m0, s3, 2
	v_cmp_gt_i32_e32 vcc, s0, v1
	v_add_u32_e32 v51, s22, v50
	s_and_saveexec_b64 s[0:1], vcc
	global_load_lds_dword v51, s[20:21]
	s_mov_b64 exec, s[0:1]
	v_readlane_b32 s22, v2, 3
	v_readlane_b32 s0, v3, 3
	v_readlane_b32 s3, v39, 3
	s_lshl_b32 s22, s22, 2
	s_add_u32 s22, s22, 0x12510
	s_lshl_b32 m0, s3, 2
	v_cmp_gt_i32_e32 vcc, s0, v1
	v_add_u32_e32 v51, s22, v50
	s_and_saveexec_b64 s[0:1], vcc
	global_load_lds_dword v51, s[20:21]
	s_mov_b64 exec, s[0:1]
	v_readlane_b32 s22, v2, 4
	v_readlane_b32 s0, v3, 4
	v_readlane_b32 s3, v39, 4
	s_lshl_b32 s22, s22, 2
	s_add_u32 s22, s22, 0x186c0
	s_lshl_b32 m0, s3, 2
	v_cmp_gt_i32_e32 vcc, s0, v1
	v_add_u32_e32 v51, s22, v50
	s_and_saveexec_b64 s[0:1], vcc
	global_load_lds_dword v51, s[20:21]
	s_mov_b64 exec, s[0:1]
	v_readlane_b32 s22, v2, 5
	v_readlane_b32 s0, v3, 5
	v_readlane_b32 s3, v39, 5
	s_lshl_b32 s22, s22, 2
	s_add_u32 s22, s22, 0x1e870
	s_lshl_b32 m0, s3, 2
	v_cmp_gt_i32_e32 vcc, s0, v1
	v_add_u32_e32 v51, s22, v50
	s_and_saveexec_b64 s[0:1], vcc
	global_load_lds_dword v51, s[20:21]
	s_mov_b64 exec, s[0:1]
	v_readlane_b32 s22, v2, 6
	v_readlane_b32 s0, v3, 6
	v_readlane_b32 s3, v39, 6
	s_lshl_b32 s22, s22, 2
	s_add_u32 s22, s22, 0x24a20
	s_lshl_b32 m0, s3, 2
	v_cmp_gt_i32_e32 vcc, s0, v1
	v_add_u32_e32 v51, s22, v50
	s_and_saveexec_b64 s[0:1], vcc
	global_load_lds_dword v51, s[20:21]
	s_mov_b64 exec, s[0:1]
	v_readlane_b32 s22, v2, 7
	v_readlane_b32 s0, v3, 7
	v_readlane_b32 s3, v39, 7
	s_lshl_b32 s22, s22, 2
	s_add_u32 s22, s22, 0x2abd0
	s_lshl_b32 m0, s3, 2
	v_cmp_gt_i32_e32 vcc, s0, v1
	v_add_u32_e32 v51, s22, v50
	s_and_saveexec_b64 s[0:1], vcc
	global_load_lds_dword v51, s[20:21]
	s_mov_b64 exec, s[0:1]
	v_readlane_b32 s22, v2, 8
	v_readlane_b32 s0, v3, 8
	v_readlane_b32 s3, v39, 8
	s_lshl_b32 s22, s22, 2
	s_add_u32 s22, s22, 0x30d80
	s_lshl_b32 m0, s3, 2
	v_cmp_gt_i32_e32 vcc, s0, v1
	v_add_u32_e32 v51, s22, v50
	s_and_saveexec_b64 s[0:1], vcc
	global_load_lds_dword v51, s[20:21]
	s_mov_b64 exec, s[0:1]
	v_readlane_b32 s22, v2, 9
	v_readlane_b32 s0, v3, 9
	v_readlane_b32 s3, v39, 9
	s_lshl_b32 s22, s22, 2
	s_add_u32 s22, s22, 0x36f30
	s_lshl_b32 m0, s3, 2
	v_cmp_gt_i32_e32 vcc, s0, v1
	v_add_u32_e32 v51, s22, v50
	s_and_saveexec_b64 s[0:1], vcc
	global_load_lds_dword v51, s[20:21]
	s_mov_b64 exec, s[0:1]
	v_readlane_b32 s22, v2, 10
	v_readlane_b32 s0, v3, 10
	v_readlane_b32 s3, v39, 10
	s_lshl_b32 s22, s22, 2
	s_add_u32 s22, s22, 0x3d0e0
	s_lshl_b32 m0, s3, 2
	v_cmp_gt_i32_e32 vcc, s0, v1
	v_add_u32_e32 v51, s22, v50
	s_and_saveexec_b64 s[0:1], vcc
	global_load_lds_dword v51, s[20:21]
	s_mov_b64 exec, s[0:1]
	v_readlane_b32 s22, v2, 11
	v_readlane_b32 s0, v3, 11
	v_readlane_b32 s3, v39, 11
	s_lshl_b32 s22, s22, 2
	s_add_u32 s22, s22, 0x43290
	s_lshl_b32 m0, s3, 2
	v_cmp_gt_i32_e32 vcc, s0, v1
	v_add_u32_e32 v51, s22, v50
	s_and_saveexec_b64 s[0:1], vcc
	global_load_lds_dword v51, s[20:21]
	s_mov_b64 exec, s[0:1]
	v_readlane_b32 s22, v2, 12
	v_readlane_b32 s0, v3, 12
	v_readlane_b32 s3, v39, 12
	s_lshl_b32 s22, s22, 2
	s_add_u32 s22, s22, 0x49440
	s_lshl_b32 m0, s3, 2
	v_cmp_gt_i32_e32 vcc, s0, v1
	v_add_u32_e32 v51, s22, v50
	s_and_saveexec_b64 s[0:1], vcc
	global_load_lds_dword v51, s[20:21]
	s_mov_b64 exec, s[0:1]
	v_readlane_b32 s22, v2, 13
	v_readlane_b32 s0, v3, 13
	v_readlane_b32 s3, v39, 13
	s_lshl_b32 s22, s22, 2
	s_add_u32 s22, s22, 0x4f5f0
	s_lshl_b32 m0, s3, 2
	v_cmp_gt_i32_e32 vcc, s0, v1
	v_add_u32_e32 v51, s22, v50
	s_and_saveexec_b64 s[0:1], vcc
	global_load_lds_dword v51, s[20:21]
	s_mov_b64 exec, s[0:1]
	v_readlane_b32 s22, v2, 14
	v_readlane_b32 s0, v3, 14
	v_readlane_b32 s3, v39, 14
	s_lshl_b32 s22, s22, 2
	s_add_u32 s22, s22, 0x557a0
	s_lshl_b32 m0, s3, 2
	v_cmp_gt_i32_e32 vcc, s0, v1
	v_add_u32_e32 v51, s22, v50
	s_and_saveexec_b64 s[0:1], vcc
	global_load_lds_dword v51, s[20:21]
	s_mov_b64 exec, s[0:1]
	v_readlane_b32 s22, v2, 15
	v_readlane_b32 s0, v3, 15
	v_readlane_b32 s3, v39, 15
	s_lshl_b32 s22, s22, 2
	s_add_u32 s22, s22, 0x5b950
	s_lshl_b32 m0, s3, 2
	v_cmp_gt_i32_e32 vcc, s0, v1
	v_add_u32_e32 v51, s22, v50
	s_and_saveexec_b64 s[0:1], vcc
	global_load_lds_dword v51, s[20:21]
	s_mov_b64 exec, s[0:1]
.LBB0_69:
	s_or_b64 exec, exec, s[0:1]
.LBB0_101:
	s_or_b64 exec, exec, s[0:1]
	s_waitcnt vmcnt(0)
	v_cmp_lt_i32_e32 vcc, 64, v3
	s_nop 0
	s_cbranch_vccz .LBB0_116
	v_mov_b32_e32 v6, 0x100
	v_lshl_or_b32 v40, v1, 2, v6
	s_mov_b32 s0, 0x61b00
	v_mov_b64_e32 v[6:7], s[20:21]
	v_mad_u64_u32 v[6:7], s[0:1], v35, s0, v[6:7]
	v_or_b32_e32 v4, 64, v1
	v_or_b32_e32 v5, 0x80, v1
	s_mov_b32 s3, 0
	s_movk_i32 s60, 0xbf
	s_movk_i32 s61, 0x186c
	v_mov_b32_e32 v9, 0
	s_mov_b64 s[0:1], 0x100
	s_mov_b64 s[22:23], 0x61b0
	s_branch .LBB0_103
